# w1 + hgrn GEMMs: As[1][1] of next unit staged before epilogue stores, first three waits of next unit relaxed to vmcnt(24); removed compiler's spurious vmcnt(0) at unit start
# baseline (speedup 1.0000x reference)
.LBB0_336:
	s_and_b32 s16, s37, 3
	s_lshl_b32 s17, s15, 13
	s_lshl_b32 s29, s16, 12
	s_add_u32 s37, s44, 0x1a100000
	s_addc_u32 s64, s45, 0
	s_add_u32 s42, s44, 0x22100000
	s_addc_u32 s43, s45, 0
	s_add_u32 s44, s44, 0x3e102000
	s_addc_u32 s45, s45, 0
	s_add_u32 s38, s58, 0x8000
	v_mov_b32_e32 v143, v115
	s_addc_u32 s39, s59, 0
	s_add_i32 m0, s13, 0x18000
	v_lshl_add_u64 v[10:11], s[38:39], 0, v[142:143]
	v_mov_b32_e32 v147, v115
	s_waitcnt vmcnt(2)
	s_barrier
	global_load_lds_dwordx4 v[10:11], off
	s_add_i32 m0, s13, 0x1a000
	v_lshl_add_u64 v[10:11], s[38:39], 0, v[146:147]
	s_add_u32 s38, s56, 0x8000
	v_mov_b32_e32 v141, v115
	s_addc_u32 s39, s57, 0
	s_add_i32 s65, s13, 0x8000
	v_mov_b32_e32 v145, v115
	global_load_lds_dwordx4 v[10:11], off
	v_lshl_add_u64 v[10:11], s[38:39], 0, v[140:141]
	s_mov_b32 m0, s65
	s_add_i32 s66, s13, 0xa000
	global_load_lds_dwordx4 v[10:11], off
	v_lshl_add_u64 v[10:11], s[38:39], 0, v[144:145]
	s_add_u32 s38, s58, 0x9000
	s_mov_b32 m0, s66
	s_addc_u32 s39, s59, 0
	global_load_lds_dwordx4 v[10:11], off
	s_add_i32 m0, s13, 0x1c000
	v_lshl_add_u64 v[10:11], s[38:39], 0, v[142:143]
	global_load_lds_dwordx4 v[10:11], off
	v_lshl_add_u64 v[10:11], s[38:39], 0, v[146:147]
	s_add_i32 m0, s13, 0x1e000
	v_and_b32_e32 v9, 15, v2
	global_load_lds_dwordx4 v[10:11], off
	v_lshrrev_b32_e32 v2, 1, v2
	v_and_b32_e32 v2, 24, v2
	v_lshlrev_b32_e32 v10, 1, v2
	v_lshl_or_b32 v173, s16, 6, v2
	v_lshlrev_b32_e32 v2, 10, v3
	v_and_b32_e32 v2, 0xfffff800, v2
	v_lshl_add_u32 v2, v4, 7, v2
	v_and_b32_e32 v3, 1, v3
	v_lshl_or_b32 v2, v3, 6, v2
	s_cmpk_lt_u32 s14, 0x100
	v_lshl_add_u32 v148, v5, 1, v2
	v_lshlrev_b32_e32 v2, 10, v6
	v_lshl_or_b32 v1, s15, 6, v9
	v_lshl_or_b32 v10, v9, 6, v10
	v_lshlrev_b32_e32 v9, 2, v9
	s_cselect_b64 s[46:47], -1, 0
	s_lshl_b32 s14, s15, 8
	v_and_b32_e32 v2, 0xfffff800, v2
	v_and_b32_e32 v11, 32, v9
	s_waitcnt vmcnt(6)
	s_add_i32 s14, s14, 0
	v_lshl_add_u32 v2, v7, 7, v2
	v_and_b32_e32 v3, 1, v6
	v_bitop3_b32 v12, v10, s17, v11 bitop3:0xde
	s_add_i32 s14, s14, 0x20400
	v_lshl_or_b32 v2, v3, 6, v2
	v_bitop3_b32 v172, v10, s29, v11 bitop3:0xde
	v_add_u32_e32 v174, s14, v9
	v_mov_b32_e32 v149, v115
	v_lshl_add_u32 v150, v8, 1, v2
	v_mov_b32_e32 v151, v115
	s_mov_b32 s14, 0
	v_add_u32_e32 v175, 0, v12
	s_mov_b32 s67, 0
	s_barrier
	s_mov_b32 s32, 0
	s_branch .LBB0_339
.LBB0_337:
	s_mov_b64 s[28:29], 0
	s_mov_b32 s32, 1

.LBB0_345:
	s_ashr_i32 s51, s50, 31
	s_lshl_b64 s[52:53], s[50:51], 20
	s_add_u32 s52, s5, s52
	s_addc_u32 s53, s8, s53
	s_and_b64 s[54:55], s[38:39], exec
	s_cselect_b32 s15, s53, s57
	s_cselect_b32 s29, s52, s56
	s_ashr_i32 s49, s48, 31
	s_lshl_b64 s[54:55], s[48:49], 20
	s_add_u32 s54, s9, s54
	s_addc_u32 s55, s12, s55
	s_and_b64 s[60:61], s[38:39], exec
	s_cselect_b32 s41, s55, s59
	s_cselect_b32 s49, s54, s58
	s_add_u32 s56, s56, 0xc000
	s_addc_u32 s57, s57, 0
	s_add_u32 s51, s58, 0x10000
	v_mov_b32_e32 v2, 0
	s_addc_u32 s69, s59, 0
	s_mov_b32 s70, -2
	v_mov_b32_e32 v3, v2
	v_mov_b32_e32 v4, v2
	v_mov_b32_e32 v5, v2
	v_mov_b32_e32 v6, v2
	v_mov_b32_e32 v7, v2
	v_mov_b32_e32 v8, v2
	v_mov_b32_e32 v9, v2
	v_mov_b32_e32 v18, v2
	v_mov_b32_e32 v19, v2
	v_mov_b32_e32 v20, v2
	v_mov_b32_e32 v21, v2
	v_mov_b32_e32 v22, v2
	v_mov_b32_e32 v23, v2
	v_mov_b32_e32 v24, v2
	v_mov_b32_e32 v25, v2
	v_mov_b32_e32 v34, v2
	v_mov_b32_e32 v35, v2
	v_mov_b32_e32 v36, v2
	v_mov_b32_e32 v37, v2
	v_mov_b32_e32 v38, v2
	v_mov_b32_e32 v39, v2
	v_mov_b32_e32 v40, v2
	v_mov_b32_e32 v41, v2
	v_mov_b32_e32 v50, v2
	v_mov_b32_e32 v51, v2
	v_mov_b32_e32 v52, v2
	v_mov_b32_e32 v53, v2
	v_mov_b32_e32 v54, v2
	v_mov_b32_e32 v55, v2
	v_mov_b32_e32 v56, v2
	v_mov_b32_e32 v57, v2
	v_mov_b32_e32 v10, v2
	v_mov_b32_e32 v11, v2
	v_mov_b32_e32 v12, v2
	v_mov_b32_e32 v13, v2
	v_mov_b32_e32 v14, v2
	v_mov_b32_e32 v15, v2
	v_mov_b32_e32 v16, v2
	v_mov_b32_e32 v17, v2
	v_mov_b32_e32 v26, v2
	v_mov_b32_e32 v27, v2
	v_mov_b32_e32 v28, v2
	v_mov_b32_e32 v29, v2
	v_mov_b32_e32 v30, v2
	v_mov_b32_e32 v31, v2
	v_mov_b32_e32 v32, v2
	v_mov_b32_e32 v33, v2
	v_mov_b32_e32 v42, v2
	v_mov_b32_e32 v43, v2
	v_mov_b32_e32 v44, v2
	v_mov_b32_e32 v45, v2
	v_mov_b32_e32 v46, v2
	v_mov_b32_e32 v47, v2
	v_mov_b32_e32 v48, v2
	v_mov_b32_e32 v49, v2
	v_mov_b32_e32 v58, v2
	v_mov_b32_e32 v59, v2
	v_mov_b32_e32 v60, v2
	v_mov_b32_e32 v61, v2
	v_mov_b32_e32 v62, v2
	v_mov_b32_e32 v63, v2
	v_mov_b32_e32 v64, v2
	v_mov_b32_e32 v65, v2
	v_mov_b32_e32 v66, v2
	v_mov_b32_e32 v67, v2
	v_mov_b32_e32 v68, v2
	v_mov_b32_e32 v69, v2
	v_mov_b32_e32 v70, v2
	v_mov_b32_e32 v71, v2
	v_mov_b32_e32 v72, v2
	v_mov_b32_e32 v73, v2
	v_mov_b32_e32 v82, v2
	v_mov_b32_e32 v83, v2
	v_mov_b32_e32 v84, v2
	v_mov_b32_e32 v85, v2
	v_mov_b32_e32 v86, v2
	v_mov_b32_e32 v87, v2
	v_mov_b32_e32 v88, v2
	v_mov_b32_e32 v89, v2
	v_mov_b32_e32 v98, v2
	v_mov_b32_e32 v99, v2
	v_mov_b32_e32 v100, v2
	v_mov_b32_e32 v101, v2
	v_mov_b32_e32 v102, v2
	v_mov_b32_e32 v103, v2
	v_mov_b32_e32 v104, v2
	v_mov_b32_e32 v105, v2
	v_mov_b32_e32 v116, v2
	v_mov_b32_e32 v117, v2
	v_mov_b32_e32 v118, v2
	v_mov_b32_e32 v119, v2
	v_mov_b32_e32 v120, v2
	v_mov_b32_e32 v121, v2
	v_mov_b32_e32 v122, v2
	v_mov_b32_e32 v123, v2
	v_mov_b32_e32 v74, v2
	v_mov_b32_e32 v75, v2
	v_mov_b32_e32 v76, v2
	v_mov_b32_e32 v77, v2
	v_mov_b32_e32 v78, v2
	v_mov_b32_e32 v79, v2
	v_mov_b32_e32 v80, v2
	v_mov_b32_e32 v81, v2
	v_mov_b32_e32 v90, v2
	v_mov_b32_e32 v91, v2
	v_mov_b32_e32 v92, v2
	v_mov_b32_e32 v93, v2
	v_mov_b32_e32 v94, v2
	v_mov_b32_e32 v95, v2
	v_mov_b32_e32 v96, v2
	v_mov_b32_e32 v97, v2
	v_mov_b32_e32 v106, v2
	v_mov_b32_e32 v107, v2
	v_mov_b32_e32 v108, v2
	v_mov_b32_e32 v109, v2
	v_mov_b32_e32 v110, v2
	v_mov_b32_e32 v111, v2
	v_mov_b32_e32 v112, v2
	v_mov_b32_e32 v113, v2
	v_mov_b32_e32 v124, v2
	v_mov_b32_e32 v125, v2
	v_mov_b32_e32 v126, v2
	v_mov_b32_e32 v127, v2
	v_mov_b32_e32 v128, v2
	v_mov_b32_e32 v129, v2
	v_mov_b32_e32 v130, v2
	v_mov_b32_e32 v131, v2
.LBB0_346:
	s_add_u32 s16, s56, 0x4000
	s_addc_u32 s17, s57, 0
	s_cmp_eq_u32 s70, 28
	s_cselect_b32 s62, s29, s16
	s_cselect_b32 s63, s15, s17
	s_cselect_b32 s61, s41, s69
	s_cselect_b32 s60, s49, s51
	s_add_u32 s58, s62, 0x8000
	s_addc_u32 s59, s63, 0
	s_add_i32 s16, 0, 0x10000
	v_add_u32_e32 v114, s16, v172
	s_add_i32 s17, 0, 0x14000
	ds_read_b128 v[132:135], v114
	ds_read_b128 v[136:139], v114 offset:1024
	s_waitcnt lgkmcnt(0)
	ds_read_b128 v[152:155], v114 offset:2048
	ds_read_b128 v[166:169], v114 offset:3072
	v_add_u32_e32 v114, s17, v172
	ds_read_b128 v[176:179], v114
	ds_read_b128 v[180:183], v114 offset:1024
	ds_read_b128 v[194:197], v114 offset:2048
	ds_read_b128 v[198:201], v114 offset:3072
	v_lshl_add_u64 v[158:159], s[56:57], 0, v[148:149]
	s_add_i32 m0, s13, 0xc000
	ds_read_b128 v[202:205], v175
	ds_read_b128 v[206:209], v175 offset:1024
	ds_read_b128 v[210:213], v175 offset:2048
	ds_read_b128 v[214:217], v175 offset:3072
	ds_read_b128 v[218:221], v175 offset:4096
	ds_read_b128 v[222:225], v175 offset:5120
	ds_read_b128 v[226:229], v175 offset:6144
	ds_read_b128 v[230:233], v175 offset:7168
	s_cmp_lg_u32 s32, 0
	s_cbranch_scc1 .Lrx_hgrn1_skip
	global_load_lds_dwordx4 v[158:159], off
	v_lshl_add_u64 v[158:159], s[56:57], 0, v[150:151]
	s_add_i32 m0, s13, 0xe000
	s_nop 0
	global_load_lds_dwordx4 v[158:159], off
.Lrx_hgrn1_skip:
	s_cmp_lg_u32 s32, 0
	s_cbranch_scc1 .Lrx_hgrn1_w0
	s_waitcnt vmcnt(8)
.Lrx_hgrn1_w0:
	s_waitcnt vmcnt(24)
	s_waitcnt lgkmcnt(0)
	s_barrier
	s_setprio 1
	s_waitcnt lgkmcnt(0)
	v_mfma_f32_16x16x32_bf16 v[128:131], v[132:135], v[202:205], v[128:131]
	v_mfma_f32_16x16x32_bf16 v[124:127], v[152:155], v[202:205], v[124:127]
	v_mfma_f32_16x16x32_bf16 v[110:113], v[132:135], v[210:213], v[110:113]
	v_mfma_f32_16x16x32_bf16 v[106:109], v[152:155], v[210:213], v[106:109]
	v_mfma_f32_16x16x32_bf16 v[94:97], v[132:135], v[218:221], v[94:97]
	v_mfma_f32_16x16x32_bf16 v[90:93], v[152:155], v[218:221], v[90:93]
	v_mfma_f32_16x16x32_bf16 v[78:81], v[132:135], v[226:229], v[78:81]
	v_mfma_f32_16x16x32_bf16 v[74:77], v[152:155], v[226:229], v[74:77]
	v_mfma_f32_16x16x32_bf16 v[128:131], v[136:139], v[206:209], v[128:131]
	v_mfma_f32_16x16x32_bf16 v[124:127], v[166:169], v[206:209], v[124:127]
	v_mfma_f32_16x16x32_bf16 v[110:113], v[136:139], v[214:217], v[110:113]
	v_mfma_f32_16x16x32_bf16 v[106:109], v[166:169], v[214:217], v[106:109]
	v_mfma_f32_16x16x32_bf16 v[94:97], v[136:139], v[222:225], v[94:97]
	v_mfma_f32_16x16x32_bf16 v[90:93], v[166:169], v[222:225], v[90:93]
	v_mfma_f32_16x16x32_bf16 v[78:81], v[136:139], v[230:233], v[78:81]
	v_mfma_f32_16x16x32_bf16 v[74:77], v[166:169], v[230:233], v[74:77]
	s_setprio 0
	s_setprio 1
	v_mfma_f32_16x16x32_bf16 v[120:123], v[176:179], v[202:205], v[120:123]
	v_mfma_f32_16x16x32_bf16 v[116:119], v[194:197], v[202:205], v[116:119]
	v_mfma_f32_16x16x32_bf16 v[102:105], v[176:179], v[210:213], v[102:105]
	v_mfma_f32_16x16x32_bf16 v[98:101], v[194:197], v[210:213], v[98:101]
	v_mfma_f32_16x16x32_bf16 v[86:89], v[176:179], v[218:221], v[86:89]
	v_mfma_f32_16x16x32_bf16 v[82:85], v[194:197], v[218:221], v[82:85]
	v_mfma_f32_16x16x32_bf16 v[70:73], v[176:179], v[226:229], v[70:73]
	v_mfma_f32_16x16x32_bf16 v[66:69], v[194:197], v[226:229], v[66:69]
	v_mfma_f32_16x16x32_bf16 v[120:123], v[180:183], v[206:209], v[120:123]
	v_mfma_f32_16x16x32_bf16 v[116:119], v[198:201], v[206:209], v[116:119]
	v_mfma_f32_16x16x32_bf16 v[102:105], v[180:183], v[214:217], v[102:105]
	v_mfma_f32_16x16x32_bf16 v[98:101], v[198:201], v[214:217], v[98:101]
	v_mfma_f32_16x16x32_bf16 v[86:89], v[180:183], v[222:225], v[86:89]
	v_mfma_f32_16x16x32_bf16 v[82:85], v[198:201], v[222:225], v[82:85]
	v_mfma_f32_16x16x32_bf16 v[70:73], v[180:183], v[230:233], v[70:73]
	v_mfma_f32_16x16x32_bf16 v[66:69], v[198:201], v[230:233], v[66:69]
	s_setprio 0
	s_barrier
	s_add_i32 s16, s16, s4
	v_lshl_add_u64 v[158:159], s[60:61], 0, v[142:143]
	s_mov_b32 m0, s16
	ds_read_b128 v[202:205], v175 offset:16384
	ds_read_b128 v[206:209], v175 offset:17408
	ds_read_b128 v[210:213], v175 offset:18432
	ds_read_b128 v[214:217], v175 offset:19456
	ds_read_b128 v[218:221], v175 offset:20480
	ds_read_b128 v[222:225], v175 offset:21504
	ds_read_b128 v[226:229], v175 offset:22528
	ds_read_b128 v[230:233], v175 offset:23552
	global_load_lds_dwordx4 v[158:159], off
	s_add_i32 m0, s16, 0x2000
	s_add_u32 s74, s60, 0x1000
	v_lshl_add_u64 v[158:159], s[60:61], 0, v[146:147]
	s_addc_u32 s75, s61, 0
	s_add_i32 s16, s17, s4
	global_load_lds_dwordx4 v[158:159], off
	v_lshl_add_u64 v[158:159], s[74:75], 0, v[142:143]
	s_mov_b32 m0, s16
	s_nop 0
	global_load_lds_dwordx4 v[158:159], off
	v_lshl_add_u64 v[158:159], s[74:75], 0, v[146:147]
	s_add_i32 m0, s16, 0x2000
	s_nop 0
	global_load_lds_dwordx4 v[158:159], off
	v_lshl_add_u64 v[158:159], s[62:63], 0, v[140:141]
	s_mov_b32 m0, s13
	s_nop 0
	global_load_lds_dwordx4 v[158:159], off
	v_lshl_add_u64 v[158:159], s[62:63], 0, v[144:145]
	s_mov_b32 m0, s20
	s_nop 0
	global_load_lds_dwordx4 v[158:159], off
	s_cmp_lg_u32 s32, 0
	s_cbranch_scc1 .Lrx_hgrn1_w1
	s_waitcnt vmcnt(8)
.Lrx_hgrn1_w1:
	s_waitcnt vmcnt(24)
	s_waitcnt lgkmcnt(0)
	s_barrier
	s_setprio 1
	s_waitcnt lgkmcnt(0)
	v_mfma_f32_16x16x32_bf16 v[62:65], v[132:135], v[202:205], v[62:65]
	v_mfma_f32_16x16x32_bf16 v[58:61], v[152:155], v[202:205], v[58:61]
	v_mfma_f32_16x16x32_bf16 v[46:49], v[132:135], v[210:213], v[46:49]
	v_mfma_f32_16x16x32_bf16 v[42:45], v[152:155], v[210:213], v[42:45]
	v_mfma_f32_16x16x32_bf16 v[30:33], v[132:135], v[218:221], v[30:33]
	v_mfma_f32_16x16x32_bf16 v[26:29], v[152:155], v[218:221], v[26:29]
	v_mfma_f32_16x16x32_bf16 v[14:17], v[132:135], v[226:229], v[14:17]
	v_mfma_f32_16x16x32_bf16 v[10:13], v[152:155], v[226:229], v[10:13]
	v_mfma_f32_16x16x32_bf16 v[62:65], v[136:139], v[206:209], v[62:65]
	v_mfma_f32_16x16x32_bf16 v[58:61], v[166:169], v[206:209], v[58:61]
	v_mfma_f32_16x16x32_bf16 v[46:49], v[136:139], v[214:217], v[46:49]
	v_mfma_f32_16x16x32_bf16 v[42:45], v[166:169], v[214:217], v[42:45]
	v_mfma_f32_16x16x32_bf16 v[30:33], v[136:139], v[222:225], v[30:33]
	v_mfma_f32_16x16x32_bf16 v[26:29], v[166:169], v[222:225], v[26:29]
	v_mfma_f32_16x16x32_bf16 v[14:17], v[136:139], v[230:233], v[14:17]
	v_mfma_f32_16x16x32_bf16 v[10:13], v[166:169], v[230:233], v[10:13]
	s_setprio 0
	s_setprio 1
	v_mfma_f32_16x16x32_bf16 v[54:57], v[176:179], v[202:205], v[54:57]
	v_mfma_f32_16x16x32_bf16 v[50:53], v[194:197], v[202:205], v[50:53]
	v_mfma_f32_16x16x32_bf16 v[38:41], v[176:179], v[210:213], v[38:41]
	v_mfma_f32_16x16x32_bf16 v[34:37], v[194:197], v[210:213], v[34:37]
	v_mfma_f32_16x16x32_bf16 v[22:25], v[176:179], v[218:221], v[22:25]
	v_mfma_f32_16x16x32_bf16 v[18:21], v[194:197], v[218:221], v[18:21]
	v_mfma_f32_16x16x32_bf16 v[6:9], v[176:179], v[226:229], v[6:9]
	v_mfma_f32_16x16x32_bf16 v[2:5], v[194:197], v[226:229], v[2:5]
	v_mfma_f32_16x16x32_bf16 v[54:57], v[180:183], v[206:209], v[54:57]
	v_mfma_f32_16x16x32_bf16 v[50:53], v[198:201], v[206:209], v[50:53]
	v_mfma_f32_16x16x32_bf16 v[38:41], v[180:183], v[214:217], v[38:41]
	v_mfma_f32_16x16x32_bf16 v[34:37], v[198:201], v[214:217], v[34:37]
	v_mfma_f32_16x16x32_bf16 v[22:25], v[180:183], v[222:225], v[22:25]
	v_mfma_f32_16x16x32_bf16 v[18:21], v[198:201], v[222:225], v[18:21]
	v_mfma_f32_16x16x32_bf16 v[6:9], v[180:183], v[230:233], v[6:9]
	v_mfma_f32_16x16x32_bf16 v[2:5], v[198:201], v[230:233], v[2:5]
	s_setprio 0
	s_barrier
	s_add_i32 s16, 0, 0x18000
	v_add_u32_e32 v114, s16, v172
	s_add_i32 s17, 0, 0x1c000
	ds_read_b128 v[132:135], v114
	ds_read_b128 v[136:139], v114 offset:1024
	ds_read_b128 v[152:155], v114 offset:2048
	ds_read_b128 v[166:169], v114 offset:3072
	v_add_u32_e32 v114, s17, v172
	ds_read_b128 v[176:179], v114
	ds_read_b128 v[180:183], v114 offset:1024
	ds_read_b128 v[194:197], v114 offset:2048
	ds_read_b128 v[198:201], v114 offset:3072
	s_add_u32 s62, s62, 0x4000
	s_addc_u32 s63, s63, 0
	s_mov_b32 m0, s21
	v_lshl_add_u64 v[158:159], s[62:63], 0, v[140:141]
	ds_read_b128 v[202:205], v175 offset:32768
	ds_read_b128 v[206:209], v175 offset:33792
	ds_read_b128 v[210:213], v175 offset:34816
	ds_read_b128 v[214:217], v175 offset:35840
	ds_read_b128 v[218:221], v175 offset:36864
	ds_read_b128 v[222:225], v175 offset:37888
	ds_read_b128 v[226:229], v175 offset:38912
	ds_read_b128 v[230:233], v175 offset:39936
	global_load_lds_dwordx4 v[158:159], off
	v_lshl_add_u64 v[158:159], s[62:63], 0, v[144:145]
	s_mov_b32 m0, s24
	s_nop 0
	global_load_lds_dwordx4 v[158:159], off
	s_cmp_lg_u32 s32, 0
	s_cbranch_scc1 .Lrx_hgrn1_w2
	s_waitcnt vmcnt(8)
.Lrx_hgrn1_w2:
	s_waitcnt vmcnt(24)
	s_mov_b32 s32, 0
	s_waitcnt lgkmcnt(0)
	s_barrier
	s_setprio 1
	s_waitcnt lgkmcnt(0)
	v_mfma_f32_16x16x32_bf16 v[128:131], v[132:135], v[202:205], v[128:131]
	v_mfma_f32_16x16x32_bf16 v[124:127], v[152:155], v[202:205], v[124:127]
	v_mfma_f32_16x16x32_bf16 v[110:113], v[132:135], v[210:213], v[110:113]
	v_mfma_f32_16x16x32_bf16 v[106:109], v[152:155], v[210:213], v[106:109]
	v_mfma_f32_16x16x32_bf16 v[94:97], v[132:135], v[218:221], v[94:97]
	v_mfma_f32_16x16x32_bf16 v[90:93], v[152:155], v[218:221], v[90:93]
	v_mfma_f32_16x16x32_bf16 v[78:81], v[132:135], v[226:229], v[78:81]
	v_mfma_f32_16x16x32_bf16 v[74:77], v[152:155], v[226:229], v[74:77]
	v_mfma_f32_16x16x32_bf16 v[128:131], v[136:139], v[206:209], v[128:131]
	v_mfma_f32_16x16x32_bf16 v[124:127], v[166:169], v[206:209], v[124:127]
	v_mfma_f32_16x16x32_bf16 v[110:113], v[136:139], v[214:217], v[110:113]
	v_mfma_f32_16x16x32_bf16 v[106:109], v[166:169], v[214:217], v[106:109]
	v_mfma_f32_16x16x32_bf16 v[94:97], v[136:139], v[222:225], v[94:97]
	v_mfma_f32_16x16x32_bf16 v[90:93], v[166:169], v[222:225], v[90:93]
	v_mfma_f32_16x16x32_bf16 v[78:81], v[136:139], v[230:233], v[78:81]
	v_mfma_f32_16x16x32_bf16 v[74:77], v[166:169], v[230:233], v[74:77]
	s_setprio 0
	s_setprio 1
	v_mfma_f32_16x16x32_bf16 v[120:123], v[176:179], v[202:205], v[120:123]
	v_mfma_f32_16x16x32_bf16 v[116:119], v[194:197], v[202:205], v[116:119]
	v_mfma_f32_16x16x32_bf16 v[102:105], v[176:179], v[210:213], v[102:105]
	v_mfma_f32_16x16x32_bf16 v[98:101], v[194:197], v[210:213], v[98:101]
	v_mfma_f32_16x16x32_bf16 v[86:89], v[176:179], v[218:221], v[86:89]
	v_mfma_f32_16x16x32_bf16 v[82:85], v[194:197], v[218:221], v[82:85]
	v_mfma_f32_16x16x32_bf16 v[70:73], v[176:179], v[226:229], v[70:73]
	v_mfma_f32_16x16x32_bf16 v[66:69], v[194:197], v[226:229], v[66:69]
	v_mfma_f32_16x16x32_bf16 v[120:123], v[180:183], v[206:209], v[120:123]
	v_mfma_f32_16x16x32_bf16 v[116:119], v[198:201], v[206:209], v[116:119]
	v_mfma_f32_16x16x32_bf16 v[102:105], v[180:183], v[214:217], v[102:105]
	v_mfma_f32_16x16x32_bf16 v[98:101], v[198:201], v[214:217], v[98:101]
	v_mfma_f32_16x16x32_bf16 v[86:89], v[180:183], v[222:225], v[86:89]
	v_mfma_f32_16x16x32_bf16 v[82:85], v[198:201], v[222:225], v[82:85]
	v_mfma_f32_16x16x32_bf16 v[70:73], v[180:183], v[230:233], v[70:73]
	v_mfma_f32_16x16x32_bf16 v[66:69], v[198:201], v[230:233], v[66:69]
	s_setprio 0
	s_barrier
	s_add_u32 s62, s60, 0x8000
	s_addc_u32 s63, s61, 0
	s_add_i32 s16, s16, s4
	v_lshl_add_u64 v[158:159], s[62:63], 0, v[142:143]
	s_mov_b32 m0, s16
	ds_read_b128 v[202:205], v175 offset:49152
	ds_read_b128 v[206:209], v175 offset:50176
	ds_read_b128 v[210:213], v175 offset:51200
	ds_read_b128 v[214:217], v175 offset:52224
	ds_read_b128 v[218:221], v175 offset:53248
	ds_read_b128 v[222:225], v175 offset:54272
	ds_read_b128 v[226:229], v175 offset:55296
	ds_read_b128 v[230:233], v175 offset:56320
	global_load_lds_dwordx4 v[158:159], off
	s_add_i32 m0, s16, 0x2000
	s_add_u32 s60, s60, 0x9000
	v_lshl_add_u64 v[158:159], s[62:63], 0, v[146:147]
	s_addc_u32 s61, s61, 0
	s_add_i32 s16, s17, s4
	global_load_lds_dwordx4 v[158:159], off
	v_lshl_add_u64 v[158:159], s[60:61], 0, v[142:143]
	s_mov_b32 m0, s16
	s_nop 0
	global_load_lds_dwordx4 v[158:159], off
	v_lshl_add_u64 v[158:159], s[60:61], 0, v[146:147]
	s_add_i32 m0, s16, 0x2000
	s_nop 0
	global_load_lds_dwordx4 v[158:159], off
	v_lshl_add_u64 v[158:159], s[58:59], 0, v[140:141]
	s_mov_b32 m0, s65
	s_nop 0
	global_load_lds_dwordx4 v[158:159], off
	v_lshl_add_u64 v[158:159], s[58:59], 0, v[144:145]
	s_mov_b32 m0, s66
	s_nop 0
	global_load_lds_dwordx4 v[158:159], off
	s_waitcnt vmcnt(8)
	s_waitcnt lgkmcnt(0)
	s_barrier
	s_setprio 1
	s_waitcnt lgkmcnt(0)
	v_mfma_f32_16x16x32_bf16 v[62:65], v[132:135], v[202:205], v[62:65]
	v_mfma_f32_16x16x32_bf16 v[58:61], v[152:155], v[202:205], v[58:61]
	v_mfma_f32_16x16x32_bf16 v[46:49], v[132:135], v[210:213], v[46:49]
	v_mfma_f32_16x16x32_bf16 v[42:45], v[152:155], v[210:213], v[42:45]
	v_mfma_f32_16x16x32_bf16 v[30:33], v[132:135], v[218:221], v[30:33]
	v_mfma_f32_16x16x32_bf16 v[26:29], v[152:155], v[218:221], v[26:29]
	v_mfma_f32_16x16x32_bf16 v[14:17], v[132:135], v[226:229], v[14:17]
	v_mfma_f32_16x16x32_bf16 v[10:13], v[152:155], v[226:229], v[10:13]
	v_mfma_f32_16x16x32_bf16 v[62:65], v[136:139], v[206:209], v[62:65]
	v_mfma_f32_16x16x32_bf16 v[58:61], v[166:169], v[206:209], v[58:61]
	v_mfma_f32_16x16x32_bf16 v[46:49], v[136:139], v[214:217], v[46:49]
	v_mfma_f32_16x16x32_bf16 v[42:45], v[166:169], v[214:217], v[42:45]
	v_mfma_f32_16x16x32_bf16 v[30:33], v[136:139], v[222:225], v[30:33]
	v_mfma_f32_16x16x32_bf16 v[26:29], v[166:169], v[222:225], v[26:29]
	v_mfma_f32_16x16x32_bf16 v[14:17], v[136:139], v[230:233], v[14:17]
	v_mfma_f32_16x16x32_bf16 v[10:13], v[166:169], v[230:233], v[10:13]
	s_setprio 0
	s_setprio 1
	v_mfma_f32_16x16x32_bf16 v[54:57], v[176:179], v[202:205], v[54:57]
	v_mfma_f32_16x16x32_bf16 v[50:53], v[194:197], v[202:205], v[50:53]
	v_mfma_f32_16x16x32_bf16 v[38:41], v[176:179], v[210:213], v[38:41]
	v_mfma_f32_16x16x32_bf16 v[34:37], v[194:197], v[210:213], v[34:37]
	v_mfma_f32_16x16x32_bf16 v[22:25], v[176:179], v[218:221], v[22:25]
	v_mfma_f32_16x16x32_bf16 v[18:21], v[194:197], v[218:221], v[18:21]
	v_mfma_f32_16x16x32_bf16 v[6:9], v[176:179], v[226:229], v[6:9]
	v_mfma_f32_16x16x32_bf16 v[2:5], v[194:197], v[226:229], v[2:5]
	v_mfma_f32_16x16x32_bf16 v[54:57], v[180:183], v[206:209], v[54:57]
	v_mfma_f32_16x16x32_bf16 v[50:53], v[198:201], v[206:209], v[50:53]
	v_mfma_f32_16x16x32_bf16 v[38:41], v[180:183], v[214:217], v[38:41]
	v_mfma_f32_16x16x32_bf16 v[34:37], v[198:201], v[214:217], v[34:37]
	v_mfma_f32_16x16x32_bf16 v[22:25], v[180:183], v[222:225], v[22:25]
	v_mfma_f32_16x16x32_bf16 v[18:21], v[198:201], v[222:225], v[18:21]
	v_mfma_f32_16x16x32_bf16 v[6:9], v[180:183], v[230:233], v[6:9]
	v_mfma_f32_16x16x32_bf16 v[2:5], v[198:201], v[230:233], v[2:5]
	s_setprio 0
	s_barrier
	s_add_i32 s70, s70, 2
	s_add_u32 s56, s56, 0x10000
	s_addc_u32 s57, s57, 0
	s_add_u32 s51, s51, 0x10000
	s_addc_u32 s69, s69, 0
	s_cmp_gt_u32 s70, 29
	s_cbranch_scc0 .LBB0_346
	s_add_u32 s100, s29, 0xc000
	s_addc_u32 s101, s15, 0
	v_lshl_add_u64 v[158:159], s[100:101], 0, v[148:149]
	s_add_i32 m0, s13, 0xc000
	s_nop 0
	global_load_lds_dwordx4 v[158:159], off
	v_lshl_add_u64 v[158:159], s[100:101], 0, v[150:151]
	s_add_i32 m0, s13, 0xe000
	s_nop 0
	global_load_lds_dwordx4 v[158:159], off
	s_and_b64 vcc, exec, s[46:47]
	s_cbranch_vccz .LBB0_349
	s_barrier

.LBB0_493:
	s_and_b32 s16, s24, 3
	s_lshl_b32 s17, s15, 13
	s_lshl_b32 s29, s16, 12
	s_add_u32 s24, s50, 0x1a100000
	s_addc_u32 s37, s51, 0
	s_add_u32 s26, s50, 0x22100000
	s_addc_u32 s27, s51, 0
	s_add_u32 s42, s50, 0x3e100000
	s_addc_u32 s43, s51, 0
	s_add_u32 s38, s56, 0x8000
	v_mov_b32_e32 v143, v115
	s_addc_u32 s39, s57, 0
	s_add_i32 m0, s12, 0x18000
	v_lshl_add_u64 v[10:11], s[38:39], 0, v[142:143]
	v_mov_b32_e32 v147, v115
	s_waitcnt vmcnt(2)
	s_barrier
	global_load_lds_dwordx4 v[10:11], off
	s_add_i32 m0, s12, 0x1a000
	v_lshl_add_u64 v[10:11], s[38:39], 0, v[146:147]
	s_add_u32 s38, s54, 0x8000
	v_mov_b32_e32 v141, v115
	s_addc_u32 s39, s55, 0
	s_add_i32 s62, s12, 0x8000
	v_mov_b32_e32 v145, v115
	global_load_lds_dwordx4 v[10:11], off
	v_lshl_add_u64 v[10:11], s[38:39], 0, v[140:141]
	s_mov_b32 m0, s62
	s_add_i32 s63, s12, 0xa000
	global_load_lds_dwordx4 v[10:11], off
	v_lshl_add_u64 v[10:11], s[38:39], 0, v[144:145]
	s_add_u32 s38, s56, 0x9000
	s_mov_b32 m0, s63
	s_addc_u32 s39, s57, 0
	global_load_lds_dwordx4 v[10:11], off
	s_add_i32 m0, s12, 0x1c000
	v_lshl_add_u64 v[10:11], s[38:39], 0, v[142:143]
	global_load_lds_dwordx4 v[10:11], off
	v_lshl_add_u64 v[10:11], s[38:39], 0, v[146:147]
	s_add_i32 m0, s12, 0x1e000
	v_and_b32_e32 v9, 15, v2
	global_load_lds_dwordx4 v[10:11], off
	v_lshrrev_b32_e32 v2, 1, v2
	v_and_b32_e32 v2, 24, v2
	v_lshlrev_b32_e32 v10, 1, v2
	v_lshl_or_b32 v173, s16, 6, v2
	v_lshlrev_b32_e32 v2, 10, v3
	v_and_b32_e32 v2, 0xfffff800, v2
	v_lshl_add_u32 v2, v4, 7, v2
	v_and_b32_e32 v3, 1, v3
	v_lshl_or_b32 v2, v3, 6, v2
	s_cmpk_lt_u32 s14, 0x100
	v_lshl_add_u32 v148, v5, 1, v2
	v_lshlrev_b32_e32 v2, 10, v6
	v_lshl_or_b32 v1, s15, 6, v9
	v_lshl_or_b32 v10, v9, 6, v10
	v_lshlrev_b32_e32 v9, 2, v9
	s_cselect_b64 s[44:45], -1, 0
	s_lshl_b32 s14, s15, 8
	v_and_b32_e32 v2, 0xfffff800, v2
	v_and_b32_e32 v11, 32, v9
	s_waitcnt vmcnt(6)
	s_add_i32 s14, s14, 0
	v_lshl_add_u32 v2, v7, 7, v2
	v_and_b32_e32 v3, 1, v6
	v_bitop3_b32 v12, v10, s17, v11 bitop3:0xde
	s_add_i32 s14, s14, 0x20400
	v_lshl_or_b32 v2, v3, 6, v2
	v_bitop3_b32 v172, v10, s29, v11 bitop3:0xde
	v_add_u32_e32 v174, s14, v9
	v_mov_b32_e32 v149, v115
	v_lshl_add_u32 v150, v8, 1, v2
	v_mov_b32_e32 v151, v115
	s_mov_b32 s14, 0
	v_add_u32_e32 v175, 0, v12
	s_mov_b32 s64, 0
	s_barrier
	s_mov_b32 s32, 0
	s_branch .LBB0_496

.LBB0_502:
	s_ashr_i32 s49, s48, 31
	s_lshl_b64 s[50:51], s[48:49], 20
	s_add_u32 s50, s5, s50
	s_addc_u32 s51, s7, s51
	s_and_b64 s[52:53], s[38:39], exec
	s_cselect_b32 s15, s51, s55
	s_cselect_b32 s29, s50, s54
	s_ashr_i32 s47, s46, 31
	s_lshl_b64 s[52:53], s[46:47], 20
	s_add_u32 s52, s8, s52
	s_addc_u32 s53, s9, s53
	s_and_b64 s[58:59], s[38:39], exec
	s_cselect_b32 s41, s53, s57
	s_cselect_b32 s47, s52, s56
	s_add_u32 s54, s54, 0xc000
	s_addc_u32 s55, s55, 0
	s_add_u32 s49, s56, 0x10000
	v_mov_b32_e32 v2, 0
	s_addc_u32 s66, s57, 0
	s_mov_b32 s67, -2
	v_mov_b32_e32 v3, v2
	v_mov_b32_e32 v4, v2
	v_mov_b32_e32 v5, v2
	v_mov_b32_e32 v6, v2
	v_mov_b32_e32 v7, v2
	v_mov_b32_e32 v8, v2
	v_mov_b32_e32 v9, v2
	v_mov_b32_e32 v18, v2
	v_mov_b32_e32 v19, v2
	v_mov_b32_e32 v20, v2
	v_mov_b32_e32 v21, v2
	v_mov_b32_e32 v22, v2
	v_mov_b32_e32 v23, v2
	v_mov_b32_e32 v24, v2
	v_mov_b32_e32 v25, v2
	v_mov_b32_e32 v34, v2
	v_mov_b32_e32 v35, v2
	v_mov_b32_e32 v36, v2
	v_mov_b32_e32 v37, v2
	v_mov_b32_e32 v38, v2
	v_mov_b32_e32 v39, v2
	v_mov_b32_e32 v40, v2
	v_mov_b32_e32 v41, v2
	v_mov_b32_e32 v50, v2
	v_mov_b32_e32 v51, v2
	v_mov_b32_e32 v52, v2
	v_mov_b32_e32 v53, v2
	v_mov_b32_e32 v54, v2
	v_mov_b32_e32 v55, v2
	v_mov_b32_e32 v56, v2
	v_mov_b32_e32 v57, v2
	v_mov_b32_e32 v10, v2
	v_mov_b32_e32 v11, v2
	v_mov_b32_e32 v12, v2
	v_mov_b32_e32 v13, v2
	v_mov_b32_e32 v14, v2
	v_mov_b32_e32 v15, v2
	v_mov_b32_e32 v16, v2
	v_mov_b32_e32 v17, v2
	v_mov_b32_e32 v26, v2
	v_mov_b32_e32 v27, v2
	v_mov_b32_e32 v28, v2
	v_mov_b32_e32 v29, v2
	v_mov_b32_e32 v30, v2
	v_mov_b32_e32 v31, v2
	v_mov_b32_e32 v32, v2
	v_mov_b32_e32 v33, v2
	v_mov_b32_e32 v42, v2
	v_mov_b32_e32 v43, v2
	v_mov_b32_e32 v44, v2
	v_mov_b32_e32 v45, v2
	v_mov_b32_e32 v46, v2
	v_mov_b32_e32 v47, v2
	v_mov_b32_e32 v48, v2
	v_mov_b32_e32 v49, v2
	v_mov_b32_e32 v58, v2
	v_mov_b32_e32 v59, v2
	v_mov_b32_e32 v60, v2
	v_mov_b32_e32 v61, v2
	v_mov_b32_e32 v62, v2
	v_mov_b32_e32 v63, v2
	v_mov_b32_e32 v64, v2
	v_mov_b32_e32 v65, v2
	v_mov_b32_e32 v66, v2
	v_mov_b32_e32 v67, v2
	v_mov_b32_e32 v68, v2
	v_mov_b32_e32 v69, v2
	v_mov_b32_e32 v70, v2
	v_mov_b32_e32 v71, v2
	v_mov_b32_e32 v72, v2
	v_mov_b32_e32 v73, v2
	v_mov_b32_e32 v82, v2
	v_mov_b32_e32 v83, v2
	v_mov_b32_e32 v84, v2
	v_mov_b32_e32 v85, v2
	v_mov_b32_e32 v86, v2
	v_mov_b32_e32 v87, v2
	v_mov_b32_e32 v88, v2
	v_mov_b32_e32 v89, v2
	v_mov_b32_e32 v98, v2
	v_mov_b32_e32 v99, v2
	v_mov_b32_e32 v100, v2
	v_mov_b32_e32 v101, v2
	v_mov_b32_e32 v102, v2
	v_mov_b32_e32 v103, v2
	v_mov_b32_e32 v104, v2
	v_mov_b32_e32 v105, v2
	v_mov_b32_e32 v116, v2
	v_mov_b32_e32 v117, v2
	v_mov_b32_e32 v118, v2
	v_mov_b32_e32 v119, v2
	v_mov_b32_e32 v120, v2
	v_mov_b32_e32 v121, v2
	v_mov_b32_e32 v122, v2
	v_mov_b32_e32 v123, v2
	v_mov_b32_e32 v74, v2
	v_mov_b32_e32 v75, v2
	v_mov_b32_e32 v76, v2
	v_mov_b32_e32 v77, v2
	v_mov_b32_e32 v78, v2
	v_mov_b32_e32 v79, v2
	v_mov_b32_e32 v80, v2
	v_mov_b32_e32 v81, v2
	v_mov_b32_e32 v90, v2
	v_mov_b32_e32 v91, v2
	v_mov_b32_e32 v92, v2
	v_mov_b32_e32 v93, v2
	v_mov_b32_e32 v94, v2
	v_mov_b32_e32 v95, v2
	v_mov_b32_e32 v96, v2
	v_mov_b32_e32 v97, v2
	v_mov_b32_e32 v106, v2
	v_mov_b32_e32 v107, v2
	v_mov_b32_e32 v108, v2
	v_mov_b32_e32 v109, v2
	v_mov_b32_e32 v110, v2
	v_mov_b32_e32 v111, v2
	v_mov_b32_e32 v112, v2
	v_mov_b32_e32 v113, v2
	v_mov_b32_e32 v124, v2
	v_mov_b32_e32 v125, v2
	v_mov_b32_e32 v126, v2
	v_mov_b32_e32 v127, v2
	v_mov_b32_e32 v128, v2
	v_mov_b32_e32 v129, v2
	v_mov_b32_e32 v130, v2
	v_mov_b32_e32 v131, v2
.LBB0_503:
	s_add_u32 s16, s54, 0x4000
	s_addc_u32 s17, s55, 0
	s_cmp_eq_u32 s67, 28
	s_cselect_b32 s60, s29, s16
	s_cselect_b32 s61, s15, s17
	s_cselect_b32 s59, s41, s66
	s_cselect_b32 s58, s47, s49
	s_add_u32 s56, s60, 0x8000
	s_addc_u32 s57, s61, 0
	s_add_i32 s16, 0, 0x10000
	v_add_u32_e32 v114, s16, v172
	s_add_i32 s17, 0, 0x14000
	ds_read_b128 v[132:135], v114
	ds_read_b128 v[136:139], v114 offset:1024
	s_waitcnt lgkmcnt(0)
	ds_read_b128 v[152:155], v114 offset:2048
	ds_read_b128 v[166:169], v114 offset:3072
	v_add_u32_e32 v114, s17, v172
	ds_read_b128 v[176:179], v114
	ds_read_b128 v[180:183], v114 offset:1024
	ds_read_b128 v[194:197], v114 offset:2048
	ds_read_b128 v[198:201], v114 offset:3072
	v_lshl_add_u64 v[158:159], s[54:55], 0, v[148:149]
	s_add_i32 m0, s12, 0xc000
	ds_read_b128 v[202:205], v175
	ds_read_b128 v[206:209], v175 offset:1024
	ds_read_b128 v[210:213], v175 offset:2048
	ds_read_b128 v[214:217], v175 offset:3072
	ds_read_b128 v[218:221], v175 offset:4096
	ds_read_b128 v[222:225], v175 offset:5120
	ds_read_b128 v[226:229], v175 offset:6144
	ds_read_b128 v[230:233], v175 offset:7168
	s_cmp_lg_u32 s32, 0
	s_cbranch_scc1 .Lrx_hgrn2_skip
	global_load_lds_dwordx4 v[158:159], off
	v_lshl_add_u64 v[158:159], s[54:55], 0, v[150:151]
	s_add_i32 m0, s12, 0xe000
	s_nop 0
	global_load_lds_dwordx4 v[158:159], off

.Lrx_hgrn2_w0:
	s_waitcnt vmcnt(24)
	s_waitcnt lgkmcnt(0)
	s_barrier
	s_setprio 1
	s_waitcnt lgkmcnt(0)
	v_mfma_f32_16x16x32_bf16 v[128:131], v[132:135], v[202:205], v[128:131]
	v_mfma_f32_16x16x32_bf16 v[124:127], v[152:155], v[202:205], v[124:127]
	v_mfma_f32_16x16x32_bf16 v[110:113], v[132:135], v[210:213], v[110:113]
	v_mfma_f32_16x16x32_bf16 v[106:109], v[152:155], v[210:213], v[106:109]
	v_mfma_f32_16x16x32_bf16 v[94:97], v[132:135], v[218:221], v[94:97]
	v_mfma_f32_16x16x32_bf16 v[90:93], v[152:155], v[218:221], v[90:93]
	v_mfma_f32_16x16x32_bf16 v[78:81], v[132:135], v[226:229], v[78:81]
	v_mfma_f32_16x16x32_bf16 v[74:77], v[152:155], v[226:229], v[74:77]
	v_mfma_f32_16x16x32_bf16 v[128:131], v[136:139], v[206:209], v[128:131]
	v_mfma_f32_16x16x32_bf16 v[124:127], v[166:169], v[206:209], v[124:127]
	v_mfma_f32_16x16x32_bf16 v[110:113], v[136:139], v[214:217], v[110:113]
	v_mfma_f32_16x16x32_bf16 v[106:109], v[166:169], v[214:217], v[106:109]
	v_mfma_f32_16x16x32_bf16 v[94:97], v[136:139], v[222:225], v[94:97]
	v_mfma_f32_16x16x32_bf16 v[90:93], v[166:169], v[222:225], v[90:93]
	v_mfma_f32_16x16x32_bf16 v[78:81], v[136:139], v[230:233], v[78:81]
	v_mfma_f32_16x16x32_bf16 v[74:77], v[166:169], v[230:233], v[74:77]
	s_setprio 0
	s_setprio 1
	v_mfma_f32_16x16x32_bf16 v[120:123], v[176:179], v[202:205], v[120:123]
	v_mfma_f32_16x16x32_bf16 v[116:119], v[194:197], v[202:205], v[116:119]
	v_mfma_f32_16x16x32_bf16 v[102:105], v[176:179], v[210:213], v[102:105]
	v_mfma_f32_16x16x32_bf16 v[98:101], v[194:197], v[210:213], v[98:101]
	v_mfma_f32_16x16x32_bf16 v[86:89], v[176:179], v[218:221], v[86:89]
	v_mfma_f32_16x16x32_bf16 v[82:85], v[194:197], v[218:221], v[82:85]
	v_mfma_f32_16x16x32_bf16 v[70:73], v[176:179], v[226:229], v[70:73]
	v_mfma_f32_16x16x32_bf16 v[66:69], v[194:197], v[226:229], v[66:69]
	v_mfma_f32_16x16x32_bf16 v[120:123], v[180:183], v[206:209], v[120:123]
	v_mfma_f32_16x16x32_bf16 v[116:119], v[198:201], v[206:209], v[116:119]
	v_mfma_f32_16x16x32_bf16 v[102:105], v[180:183], v[214:217], v[102:105]
	v_mfma_f32_16x16x32_bf16 v[98:101], v[198:201], v[214:217], v[98:101]
	v_mfma_f32_16x16x32_bf16 v[86:89], v[180:183], v[222:225], v[86:89]
	v_mfma_f32_16x16x32_bf16 v[82:85], v[198:201], v[222:225], v[82:85]
	v_mfma_f32_16x16x32_bf16 v[70:73], v[180:183], v[230:233], v[70:73]
	v_mfma_f32_16x16x32_bf16 v[66:69], v[198:201], v[230:233], v[66:69]
	s_setprio 0
	s_barrier
	s_add_i32 s16, s16, s4
	v_lshl_add_u64 v[158:159], s[58:59], 0, v[142:143]
	s_mov_b32 m0, s16
	ds_read_b128 v[202:205], v175 offset:16384
	ds_read_b128 v[206:209], v175 offset:17408
	ds_read_b128 v[210:213], v175 offset:18432
	ds_read_b128 v[214:217], v175 offset:19456
	ds_read_b128 v[218:221], v175 offset:20480
	ds_read_b128 v[222:225], v175 offset:21504
	ds_read_b128 v[226:229], v175 offset:22528
	ds_read_b128 v[230:233], v175 offset:23552
	global_load_lds_dwordx4 v[158:159], off
	s_add_i32 m0, s16, 0x2000
	s_add_u32 s68, s58, 0x1000
	v_lshl_add_u64 v[158:159], s[58:59], 0, v[146:147]
	s_addc_u32 s69, s59, 0
	s_add_i32 s16, s17, s4
	global_load_lds_dwordx4 v[158:159], off
	v_lshl_add_u64 v[158:159], s[68:69], 0, v[142:143]
	s_mov_b32 m0, s16
	s_nop 0
	global_load_lds_dwordx4 v[158:159], off
	v_lshl_add_u64 v[158:159], s[68:69], 0, v[146:147]
	s_add_i32 m0, s16, 0x2000
	s_nop 0
	global_load_lds_dwordx4 v[158:159], off
	v_lshl_add_u64 v[158:159], s[60:61], 0, v[140:141]
	s_mov_b32 m0, s12
	s_nop 0
	global_load_lds_dwordx4 v[158:159], off
	v_lshl_add_u64 v[158:159], s[60:61], 0, v[144:145]
	s_mov_b32 m0, s13
	s_nop 0
	global_load_lds_dwordx4 v[158:159], off
	s_cmp_lg_u32 s32, 0
	s_cbranch_scc1 .Lrx_hgrn2_w1
	s_waitcnt vmcnt(8)
.Lrx_hgrn2_w1:
	s_waitcnt vmcnt(24)
	s_waitcnt lgkmcnt(0)
	s_barrier
	s_setprio 1
	s_waitcnt lgkmcnt(0)
	v_mfma_f32_16x16x32_bf16 v[62:65], v[132:135], v[202:205], v[62:65]
	v_mfma_f32_16x16x32_bf16 v[58:61], v[152:155], v[202:205], v[58:61]
	v_mfma_f32_16x16x32_bf16 v[46:49], v[132:135], v[210:213], v[46:49]
	v_mfma_f32_16x16x32_bf16 v[42:45], v[152:155], v[210:213], v[42:45]
	v_mfma_f32_16x16x32_bf16 v[30:33], v[132:135], v[218:221], v[30:33]
	v_mfma_f32_16x16x32_bf16 v[26:29], v[152:155], v[218:221], v[26:29]
	v_mfma_f32_16x16x32_bf16 v[14:17], v[132:135], v[226:229], v[14:17]
	v_mfma_f32_16x16x32_bf16 v[10:13], v[152:155], v[226:229], v[10:13]
	v_mfma_f32_16x16x32_bf16 v[62:65], v[136:139], v[206:209], v[62:65]
	v_mfma_f32_16x16x32_bf16 v[58:61], v[166:169], v[206:209], v[58:61]
	v_mfma_f32_16x16x32_bf16 v[46:49], v[136:139], v[214:217], v[46:49]
	v_mfma_f32_16x16x32_bf16 v[42:45], v[166:169], v[214:217], v[42:45]
	v_mfma_f32_16x16x32_bf16 v[30:33], v[136:139], v[222:225], v[30:33]
	v_mfma_f32_16x16x32_bf16 v[26:29], v[166:169], v[222:225], v[26:29]
	v_mfma_f32_16x16x32_bf16 v[14:17], v[136:139], v[230:233], v[14:17]
	v_mfma_f32_16x16x32_bf16 v[10:13], v[166:169], v[230:233], v[10:13]
	s_setprio 0
	s_setprio 1
	v_mfma_f32_16x16x32_bf16 v[54:57], v[176:179], v[202:205], v[54:57]
	v_mfma_f32_16x16x32_bf16 v[50:53], v[194:197], v[202:205], v[50:53]
	v_mfma_f32_16x16x32_bf16 v[38:41], v[176:179], v[210:213], v[38:41]
	v_mfma_f32_16x16x32_bf16 v[34:37], v[194:197], v[210:213], v[34:37]
	v_mfma_f32_16x16x32_bf16 v[22:25], v[176:179], v[218:221], v[22:25]
	v_mfma_f32_16x16x32_bf16 v[18:21], v[194:197], v[218:221], v[18:21]
	v_mfma_f32_16x16x32_bf16 v[6:9], v[176:179], v[226:229], v[6:9]
	v_mfma_f32_16x16x32_bf16 v[2:5], v[194:197], v[226:229], v[2:5]
	v_mfma_f32_16x16x32_bf16 v[54:57], v[180:183], v[206:209], v[54:57]
	v_mfma_f32_16x16x32_bf16 v[50:53], v[198:201], v[206:209], v[50:53]
	v_mfma_f32_16x16x32_bf16 v[38:41], v[180:183], v[214:217], v[38:41]
	v_mfma_f32_16x16x32_bf16 v[34:37], v[198:201], v[214:217], v[34:37]
	v_mfma_f32_16x16x32_bf16 v[22:25], v[180:183], v[222:225], v[22:25]
	v_mfma_f32_16x16x32_bf16 v[18:21], v[198:201], v[222:225], v[18:21]
	v_mfma_f32_16x16x32_bf16 v[6:9], v[180:183], v[230:233], v[6:9]
	v_mfma_f32_16x16x32_bf16 v[2:5], v[198:201], v[230:233], v[2:5]
	s_setprio 0
	s_barrier
	s_add_i32 s16, 0, 0x18000
	v_add_u32_e32 v114, s16, v172
	s_add_i32 s17, 0, 0x1c000
	ds_read_b128 v[132:135], v114
	ds_read_b128 v[136:139], v114 offset:1024
	ds_read_b128 v[152:155], v114 offset:2048
	ds_read_b128 v[166:169], v114 offset:3072
	v_add_u32_e32 v114, s17, v172
	ds_read_b128 v[176:179], v114
	ds_read_b128 v[180:183], v114 offset:1024
	ds_read_b128 v[194:197], v114 offset:2048
	ds_read_b128 v[198:201], v114 offset:3072
	s_add_u32 s60, s60, 0x4000
	s_addc_u32 s61, s61, 0
	s_mov_b32 m0, s20
	v_lshl_add_u64 v[158:159], s[60:61], 0, v[140:141]
	ds_read_b128 v[202:205], v175 offset:32768
	ds_read_b128 v[206:209], v175 offset:33792
	ds_read_b128 v[210:213], v175 offset:34816
	ds_read_b128 v[214:217], v175 offset:35840
	ds_read_b128 v[218:221], v175 offset:36864
	ds_read_b128 v[222:225], v175 offset:37888
	ds_read_b128 v[226:229], v175 offset:38912
	ds_read_b128 v[230:233], v175 offset:39936
	global_load_lds_dwordx4 v[158:159], off
	v_lshl_add_u64 v[158:159], s[60:61], 0, v[144:145]
	s_mov_b32 m0, s21
	s_nop 0
	global_load_lds_dwordx4 v[158:159], off
	s_cmp_lg_u32 s32, 0
	s_cbranch_scc1 .Lrx_hgrn2_w2
	s_waitcnt vmcnt(8)
.Lrx_hgrn2_w2:
	s_waitcnt vmcnt(24)
	s_mov_b32 s32, 0
	s_waitcnt lgkmcnt(0)
	s_barrier
	s_setprio 1
	s_waitcnt lgkmcnt(0)
	v_mfma_f32_16x16x32_bf16 v[128:131], v[132:135], v[202:205], v[128:131]
	v_mfma_f32_16x16x32_bf16 v[124:127], v[152:155], v[202:205], v[124:127]
	v_mfma_f32_16x16x32_bf16 v[110:113], v[132:135], v[210:213], v[110:113]
	v_mfma_f32_16x16x32_bf16 v[106:109], v[152:155], v[210:213], v[106:109]
	v_mfma_f32_16x16x32_bf16 v[94:97], v[132:135], v[218:221], v[94:97]
	v_mfma_f32_16x16x32_bf16 v[90:93], v[152:155], v[218:221], v[90:93]
	v_mfma_f32_16x16x32_bf16 v[78:81], v[132:135], v[226:229], v[78:81]
	v_mfma_f32_16x16x32_bf16 v[74:77], v[152:155], v[226:229], v[74:77]
	v_mfma_f32_16x16x32_bf16 v[128:131], v[136:139], v[206:209], v[128:131]
	v_mfma_f32_16x16x32_bf16 v[124:127], v[166:169], v[206:209], v[124:127]
	v_mfma_f32_16x16x32_bf16 v[110:113], v[136:139], v[214:217], v[110:113]
	v_mfma_f32_16x16x32_bf16 v[106:109], v[166:169], v[214:217], v[106:109]
	v_mfma_f32_16x16x32_bf16 v[94:97], v[136:139], v[222:225], v[94:97]
	v_mfma_f32_16x16x32_bf16 v[90:93], v[166:169], v[222:225], v[90:93]
	v_mfma_f32_16x16x32_bf16 v[78:81], v[136:139], v[230:233], v[78:81]
	v_mfma_f32_16x16x32_bf16 v[74:77], v[166:169], v[230:233], v[74:77]
	s_setprio 0
	s_setprio 1
	v_mfma_f32_16x16x32_bf16 v[120:123], v[176:179], v[202:205], v[120:123]
	v_mfma_f32_16x16x32_bf16 v[116:119], v[194:197], v[202:205], v[116:119]
	v_mfma_f32_16x16x32_bf16 v[102:105], v[176:179], v[210:213], v[102:105]
	v_mfma_f32_16x16x32_bf16 v[98:101], v[194:197], v[210:213], v[98:101]
	v_mfma_f32_16x16x32_bf16 v[86:89], v[176:179], v[218:221], v[86:89]
	v_mfma_f32_16x16x32_bf16 v[82:85], v[194:197], v[218:221], v[82:85]
	v_mfma_f32_16x16x32_bf16 v[70:73], v[176:179], v[226:229], v[70:73]
	v_mfma_f32_16x16x32_bf16 v[66:69], v[194:197], v[226:229], v[66:69]
	v_mfma_f32_16x16x32_bf16 v[120:123], v[180:183], v[206:209], v[120:123]
	v_mfma_f32_16x16x32_bf16 v[116:119], v[198:201], v[206:209], v[116:119]
	v_mfma_f32_16x16x32_bf16 v[102:105], v[180:183], v[214:217], v[102:105]
	v_mfma_f32_16x16x32_bf16 v[98:101], v[198:201], v[214:217], v[98:101]
	v_mfma_f32_16x16x32_bf16 v[86:89], v[180:183], v[222:225], v[86:89]
	v_mfma_f32_16x16x32_bf16 v[82:85], v[198:201], v[222:225], v[82:85]
	v_mfma_f32_16x16x32_bf16 v[70:73], v[180:183], v[230:233], v[70:73]
	v_mfma_f32_16x16x32_bf16 v[66:69], v[198:201], v[230:233], v[66:69]
	s_setprio 0
	s_barrier
	s_add_u32 s60, s58, 0x8000
	s_addc_u32 s61, s59, 0
	s_add_i32 s16, s16, s4
	v_lshl_add_u64 v[158:159], s[60:61], 0, v[142:143]
	s_mov_b32 m0, s16
	ds_read_b128 v[202:205], v175 offset:49152
	ds_read_b128 v[206:209], v175 offset:50176
	ds_read_b128 v[210:213], v175 offset:51200
	ds_read_b128 v[214:217], v175 offset:52224
	ds_read_b128 v[218:221], v175 offset:53248
	ds_read_b128 v[222:225], v175 offset:54272
	ds_read_b128 v[226:229], v175 offset:55296
	ds_read_b128 v[230:233], v175 offset:56320
	global_load_lds_dwordx4 v[158:159], off
	s_add_i32 m0, s16, 0x2000
	s_add_u32 s58, s58, 0x9000
	v_lshl_add_u64 v[158:159], s[60:61], 0, v[146:147]
	s_addc_u32 s59, s59, 0
	s_add_i32 s16, s17, s4
	global_load_lds_dwordx4 v[158:159], off
	v_lshl_add_u64 v[158:159], s[58:59], 0, v[142:143]
	s_mov_b32 m0, s16
	s_nop 0
	global_load_lds_dwordx4 v[158:159], off
	v_lshl_add_u64 v[158:159], s[58:59], 0, v[146:147]
	s_add_i32 m0, s16, 0x2000
	s_nop 0
	global_load_lds_dwordx4 v[158:159], off
	v_lshl_add_u64 v[158:159], s[56:57], 0, v[140:141]
	s_mov_b32 m0, s62
	s_nop 0
	global_load_lds_dwordx4 v[158:159], off
	v_lshl_add_u64 v[158:159], s[56:57], 0, v[144:145]
	s_mov_b32 m0, s63
	s_nop 0
	global_load_lds_dwordx4 v[158:159], off
	s_waitcnt vmcnt(8)
	s_waitcnt lgkmcnt(0)
	s_barrier
	s_setprio 1
	s_waitcnt lgkmcnt(0)
	v_mfma_f32_16x16x32_bf16 v[62:65], v[132:135], v[202:205], v[62:65]
	v_mfma_f32_16x16x32_bf16 v[58:61], v[152:155], v[202:205], v[58:61]
	v_mfma_f32_16x16x32_bf16 v[46:49], v[132:135], v[210:213], v[46:49]
	v_mfma_f32_16x16x32_bf16 v[42:45], v[152:155], v[210:213], v[42:45]
	v_mfma_f32_16x16x32_bf16 v[30:33], v[132:135], v[218:221], v[30:33]
	v_mfma_f32_16x16x32_bf16 v[26:29], v[152:155], v[218:221], v[26:29]
	v_mfma_f32_16x16x32_bf16 v[14:17], v[132:135], v[226:229], v[14:17]
	v_mfma_f32_16x16x32_bf16 v[10:13], v[152:155], v[226:229], v[10:13]
	v_mfma_f32_16x16x32_bf16 v[62:65], v[136:139], v[206:209], v[62:65]
	v_mfma_f32_16x16x32_bf16 v[58:61], v[166:169], v[206:209], v[58:61]
	v_mfma_f32_16x16x32_bf16 v[46:49], v[136:139], v[214:217], v[46:49]
	v_mfma_f32_16x16x32_bf16 v[42:45], v[166:169], v[214:217], v[42:45]
	v_mfma_f32_16x16x32_bf16 v[30:33], v[136:139], v[222:225], v[30:33]
	v_mfma_f32_16x16x32_bf16 v[26:29], v[166:169], v[222:225], v[26:29]
	v_mfma_f32_16x16x32_bf16 v[14:17], v[136:139], v[230:233], v[14:17]
	v_mfma_f32_16x16x32_bf16 v[10:13], v[166:169], v[230:233], v[10:13]
	s_setprio 0
	s_setprio 1
	v_mfma_f32_16x16x32_bf16 v[54:57], v[176:179], v[202:205], v[54:57]
	v_mfma_f32_16x16x32_bf16 v[50:53], v[194:197], v[202:205], v[50:53]
	v_mfma_f32_16x16x32_bf16 v[38:41], v[176:179], v[210:213], v[38:41]
	v_mfma_f32_16x16x32_bf16 v[34:37], v[194:197], v[210:213], v[34:37]
	v_mfma_f32_16x16x32_bf16 v[22:25], v[176:179], v[218:221], v[22:25]
	v_mfma_f32_16x16x32_bf16 v[18:21], v[194:197], v[218:221], v[18:21]
	v_mfma_f32_16x16x32_bf16 v[6:9], v[176:179], v[226:229], v[6:9]
	v_mfma_f32_16x16x32_bf16 v[2:5], v[194:197], v[226:229], v[2:5]
	v_mfma_f32_16x16x32_bf16 v[54:57], v[180:183], v[206:209], v[54:57]
	v_mfma_f32_16x16x32_bf16 v[50:53], v[198:201], v[206:209], v[50:53]
	v_mfma_f32_16x16x32_bf16 v[38:41], v[180:183], v[214:217], v[38:41]
	v_mfma_f32_16x16x32_bf16 v[34:37], v[198:201], v[214:217], v[34:37]
	v_mfma_f32_16x16x32_bf16 v[22:25], v[180:183], v[222:225], v[22:25]
	v_mfma_f32_16x16x32_bf16 v[18:21], v[198:201], v[222:225], v[18:21]
	v_mfma_f32_16x16x32_bf16 v[6:9], v[180:183], v[230:233], v[6:9]
	v_mfma_f32_16x16x32_bf16 v[2:5], v[198:201], v[230:233], v[2:5]
	s_setprio 0
	s_barrier
	s_add_i32 s67, s67, 2
	s_add_u32 s54, s54, 0x10000
	s_addc_u32 s55, s55, 0
	s_add_u32 s49, s49, 0x10000
	s_addc_u32 s66, s66, 0
	s_cmp_gt_u32 s67, 29
	s_cbranch_scc0 .LBB0_503
	s_add_u32 s100, s29, 0xc000
	s_addc_u32 s101, s15, 0
	v_lshl_add_u64 v[158:159], s[100:101], 0, v[148:149]
	s_add_i32 m0, s12, 0xc000
	s_nop 0
	global_load_lds_dwordx4 v[158:159], off
	v_lshl_add_u64 v[158:159], s[100:101], 0, v[150:151]
	s_add_i32 m0, s12, 0xe000
	s_nop 0
	global_load_lds_dwordx4 v[158:159], off
	s_and_b64 vcc, exec, s[44:45]
	s_cbranch_vccz .LBB0_506
	s_barrier

.LBB0_1220:
	v_and_b32_e32 v9, 15, v1
	v_and_b32_e32 v8, 48, v1
	v_lshlrev_b32_e32 v12, 2, v9
	s_sext_i32_i8 s58, s10
	s_and_b32 s45, s29, 3
	v_lshl_or_b32 v1, v9, 6, v8
	s_lshl_b32 s10, s28, 13
	v_and_b32_e32 v10, 32, v12
	s_lshl_b32 s29, s28, 6
	v_bitop3_b32 v13, v1, s10, v10 bitop3:0xde
	s_lshl_b32 s10, s45, 12
	s_add_u32 s16, s48, 0x8000
	s_addc_u32 s17, s49, 0
	v_bitop3_b32 v1, v1, s10, v10 bitop3:0xde
	s_add_i32 m0, s20, 0x18000
	v_lshl_add_u64 v[10:11], s[16:17], 0, v[114:115]
	v_mov_b32_e32 v137, v115
	s_waitcnt vmcnt(2)
	s_barrier
	global_load_lds_dwordx4 v[10:11], off
	s_add_i32 m0, s20, 0x1a000
	v_lshl_add_u64 v[10:11], s[16:17], 0, v[136:137]
	s_add_u32 s16, s46, 0x8000
	v_mov_b32_e32 v133, v115
	s_addc_u32 s17, s47, 0
	s_add_i32 s54, s20, 0x8000
	v_mov_b32_e32 v135, v115
	global_load_lds_dwordx4 v[10:11], off
	v_lshl_add_u64 v[10:11], s[16:17], 0, v[132:133]
	s_mov_b32 m0, s54
	s_add_i32 s55, s20, 0xa000
	global_load_lds_dwordx4 v[10:11], off
	v_lshl_add_u64 v[10:11], s[16:17], 0, v[134:135]
	s_add_u32 s16, s48, 0x9000
	s_mov_b32 m0, s55
	s_addc_u32 s17, s49, 0
	global_load_lds_dwordx4 v[10:11], off
	s_add_i32 m0, s20, 0x1c000
	v_lshl_add_u64 v[10:11], s[16:17], 0, v[114:115]
	global_load_lds_dwordx4 v[10:11], off
	v_lshl_add_u64 v[10:11], s[16:17], 0, v[136:137]
	s_add_i32 m0, s20, 0x1e000
	s_cmpk_lt_u32 s11, 0x100
	global_load_lds_dwordx4 v[10:11], off
	s_cselect_b64 s[10:11], -1, 0
	s_ashr_i32 s16, s29, 31
	v_or_b32_e32 v10, s29, v9
	v_mov_b32_e32 v11, s16
	v_lshlrev_b64 v[10:11], 7, v[10:11]
	v_lshl_add_u64 v[10:11], s[26:27], 0, v[10:11]
	v_mov_b32_e32 v9, v115
	v_lshl_add_u64 v[8:9], v[10:11], 0, v[8:9]
	s_mov_b64 s[16:17], 0x28100000
	v_lshl_add_u64 v[138:139], v[8:9], 0, s[16:17]
	v_lshlrev_b32_e32 v8, 10, v2
	v_and_b32_e32 v8, 0xfffff800, v8
	v_lshl_add_u32 v3, v3, 7, v8
	v_and_b32_e32 v2, 1, v2
	v_lshl_or_b32 v2, v2, 6, v3
	v_lshl_add_u32 v140, v4, 1, v2
	v_lshlrev_b32_e32 v2, 10, v5
	s_lshl_b32 s16, s28, 8
	v_and_b32_e32 v2, 0xfffff800, v2
	s_waitcnt vmcnt(6)
	s_add_i32 s16, s16, 0
	v_lshl_add_u32 v2, v6, 7, v2
	v_and_b32_e32 v3, 1, v5
	s_add_i32 s16, s16, 0x20400
	v_lshl_or_b32 v2, v3, 6, v2
	v_add_u32_e32 v146, s16, v12
	v_mov_b32_e32 v141, v115
	v_lshl_add_u32 v142, v7, 1, v2
	v_mov_b32_e32 v143, v115
	s_mov_b32 s59, 0
	v_add_u32_e32 v147, 0, v13
	s_mov_b32 s56, 0
	s_barrier
	s_mov_b32 s32, 0
	s_branch .LBB0_1223

.LBB0_1230:
	s_add_u32 s16, s46, 0x4000
	s_addc_u32 s17, s47, 0
	s_cmp_eq_u32 s64, 28
	s_cselect_b32 s52, s60, s16
	s_cselect_b32 s53, s29, s17
	s_cselect_b32 s51, s27, s63
	s_cselect_b32 s50, s61, s62
	s_add_u32 s48, s52, 0x8000
	s_addc_u32 s49, s53, 0
	s_add_i32 s16, 0, 0x10000
	v_add_u32_e32 v144, s16, v1
	s_add_i32 s65, 0, 0x14000
	ds_read_b128 v[148:151], v144
	ds_read_b128 v[152:155], v144 offset:1024
	ds_read_b128 v[158:161], v144 offset:2048
	ds_read_b128 v[166:169], v144 offset:3072
	v_add_u32_e32 v144, s65, v1
	ds_read_b128 v[170:173], v144
	ds_read_b128 v[174:177], v144 offset:1024
	ds_read_b128 v[178:181], v144 offset:2048
	ds_read_b128 v[194:197], v144 offset:3072
	v_lshl_add_u64 v[144:145], s[46:47], 0, v[140:141]
	s_add_i32 m0, s20, 0xc000
	ds_read_b128 v[198:201], v147
	ds_read_b128 v[202:205], v147 offset:1024
	ds_read_b128 v[206:209], v147 offset:2048
	ds_read_b128 v[210:213], v147 offset:3072
	ds_read_b128 v[214:217], v147 offset:4096
	ds_read_b128 v[218:221], v147 offset:5120
	ds_read_b128 v[222:225], v147 offset:6144
	ds_read_b128 v[226:229], v147 offset:7168
	s_cmp_lg_u32 s32, 0
	s_cbranch_scc1 .Lrx_relu2_skip
	global_load_lds_dwordx4 v[144:145], off
	v_lshl_add_u64 v[144:145], s[46:47], 0, v[142:143]
	s_add_i32 m0, s20, 0xe000
	s_nop 0
	global_load_lds_dwordx4 v[144:145], off

.Lrx_relu2_w1:
	s_waitcnt vmcnt(24)
	s_waitcnt lgkmcnt(0)
	s_barrier
	s_setprio 1
	s_waitcnt lgkmcnt(0)
	v_mfma_f32_16x16x32_bf16 v[62:65], v[148:151], v[198:201], v[62:65]
	v_mfma_f32_16x16x32_bf16 v[58:61], v[158:161], v[198:201], v[58:61]
	v_mfma_f32_16x16x32_bf16 v[46:49], v[148:151], v[206:209], v[46:49]
	v_mfma_f32_16x16x32_bf16 v[42:45], v[158:161], v[206:209], v[42:45]
	v_mfma_f32_16x16x32_bf16 v[30:33], v[148:151], v[214:217], v[30:33]
	v_mfma_f32_16x16x32_bf16 v[26:29], v[158:161], v[214:217], v[26:29]
	v_mfma_f32_16x16x32_bf16 v[14:17], v[148:151], v[222:225], v[14:17]
	v_mfma_f32_16x16x32_bf16 v[10:13], v[158:161], v[222:225], v[10:13]
	v_mfma_f32_16x16x32_bf16 v[62:65], v[152:155], v[202:205], v[62:65]
	v_mfma_f32_16x16x32_bf16 v[58:61], v[166:169], v[202:205], v[58:61]
	v_mfma_f32_16x16x32_bf16 v[46:49], v[152:155], v[210:213], v[46:49]
	v_mfma_f32_16x16x32_bf16 v[42:45], v[166:169], v[210:213], v[42:45]
	v_mfma_f32_16x16x32_bf16 v[30:33], v[152:155], v[218:221], v[30:33]
	v_mfma_f32_16x16x32_bf16 v[26:29], v[166:169], v[218:221], v[26:29]
	v_mfma_f32_16x16x32_bf16 v[14:17], v[152:155], v[226:229], v[14:17]
	v_mfma_f32_16x16x32_bf16 v[10:13], v[166:169], v[226:229], v[10:13]
	s_setprio 0
	s_setprio 1
	v_mfma_f32_16x16x32_bf16 v[54:57], v[170:173], v[198:201], v[54:57]
	v_mfma_f32_16x16x32_bf16 v[50:53], v[178:181], v[198:201], v[50:53]
	v_mfma_f32_16x16x32_bf16 v[38:41], v[170:173], v[206:209], v[38:41]
	v_mfma_f32_16x16x32_bf16 v[34:37], v[178:181], v[206:209], v[34:37]
	v_mfma_f32_16x16x32_bf16 v[22:25], v[170:173], v[214:217], v[22:25]
	v_mfma_f32_16x16x32_bf16 v[18:21], v[178:181], v[214:217], v[18:21]
	v_mfma_f32_16x16x32_bf16 v[6:9], v[170:173], v[222:225], v[6:9]
	v_mfma_f32_16x16x32_bf16 v[2:5], v[178:181], v[222:225], v[2:5]
	v_mfma_f32_16x16x32_bf16 v[54:57], v[174:177], v[202:205], v[54:57]
	v_mfma_f32_16x16x32_bf16 v[50:53], v[194:197], v[202:205], v[50:53]
	v_mfma_f32_16x16x32_bf16 v[38:41], v[174:177], v[210:213], v[38:41]
	v_mfma_f32_16x16x32_bf16 v[34:37], v[194:197], v[210:213], v[34:37]
	v_mfma_f32_16x16x32_bf16 v[22:25], v[174:177], v[218:221], v[22:25]
	v_mfma_f32_16x16x32_bf16 v[18:21], v[194:197], v[218:221], v[18:21]
	v_mfma_f32_16x16x32_bf16 v[6:9], v[174:177], v[226:229], v[6:9]
	v_mfma_f32_16x16x32_bf16 v[2:5], v[194:197], v[226:229], v[2:5]
	s_setprio 0
	s_barrier
	s_add_i32 s65, 0, 0x18000
	v_add_u32_e32 v144, s65, v1
	s_add_i32 s66, 0, 0x1c000
	ds_read_b128 v[148:151], v144
	ds_read_b128 v[152:155], v144 offset:1024
	ds_read_b128 v[158:161], v144 offset:2048
	ds_read_b128 v[166:169], v144 offset:3072
	v_add_u32_e32 v144, s66, v1
	ds_read_b128 v[170:173], v144
	ds_read_b128 v[174:177], v144 offset:1024
	ds_read_b128 v[178:181], v144 offset:2048
	ds_read_b128 v[194:197], v144 offset:3072
	s_add_u32 s16, s52, 0x4000
	s_addc_u32 s17, s53, 0
	s_mov_b32 m0, s24
	v_lshl_add_u64 v[144:145], s[16:17], 0, v[132:133]
	ds_read_b128 v[198:201], v147 offset:32768
	ds_read_b128 v[202:205], v147 offset:33792
	ds_read_b128 v[206:209], v147 offset:34816
	ds_read_b128 v[210:213], v147 offset:35840
	ds_read_b128 v[214:217], v147 offset:36864
	ds_read_b128 v[218:221], v147 offset:37888
	ds_read_b128 v[222:225], v147 offset:38912
	ds_read_b128 v[226:229], v147 offset:39936
	global_load_lds_dwordx4 v[144:145], off
	v_lshl_add_u64 v[144:145], s[16:17], 0, v[134:135]
	s_mov_b32 m0, s37
	s_nop 0
	global_load_lds_dwordx4 v[144:145], off
	s_cmp_lg_u32 s32, 0
	s_cbranch_scc1 .Lrx_relu2_w2
	s_waitcnt vmcnt(8)
.Lrx_relu2_w2:
	s_waitcnt vmcnt(24)
	s_mov_b32 s32, 0
	s_waitcnt lgkmcnt(0)
	s_barrier
	s_setprio 1
	s_waitcnt lgkmcnt(0)
	v_mfma_f32_16x16x32_bf16 v[128:131], v[148:151], v[198:201], v[128:131]
	v_mfma_f32_16x16x32_bf16 v[124:127], v[158:161], v[198:201], v[124:127]
	v_mfma_f32_16x16x32_bf16 v[110:113], v[148:151], v[206:209], v[110:113]
	v_mfma_f32_16x16x32_bf16 v[106:109], v[158:161], v[206:209], v[106:109]
	v_mfma_f32_16x16x32_bf16 v[94:97], v[148:151], v[214:217], v[94:97]
	v_mfma_f32_16x16x32_bf16 v[90:93], v[158:161], v[214:217], v[90:93]
	v_mfma_f32_16x16x32_bf16 v[78:81], v[148:151], v[222:225], v[78:81]
	v_mfma_f32_16x16x32_bf16 v[74:77], v[158:161], v[222:225], v[74:77]
	v_mfma_f32_16x16x32_bf16 v[128:131], v[152:155], v[202:205], v[128:131]
	v_mfma_f32_16x16x32_bf16 v[124:127], v[166:169], v[202:205], v[124:127]
	v_mfma_f32_16x16x32_bf16 v[110:113], v[152:155], v[210:213], v[110:113]
	v_mfma_f32_16x16x32_bf16 v[106:109], v[166:169], v[210:213], v[106:109]
	v_mfma_f32_16x16x32_bf16 v[94:97], v[152:155], v[218:221], v[94:97]
	v_mfma_f32_16x16x32_bf16 v[90:93], v[166:169], v[218:221], v[90:93]
	v_mfma_f32_16x16x32_bf16 v[78:81], v[152:155], v[226:229], v[78:81]
	v_mfma_f32_16x16x32_bf16 v[74:77], v[166:169], v[226:229], v[74:77]
	s_setprio 0
	s_setprio 1
	v_mfma_f32_16x16x32_bf16 v[120:123], v[170:173], v[198:201], v[120:123]
	v_mfma_f32_16x16x32_bf16 v[116:119], v[178:181], v[198:201], v[116:119]
	v_mfma_f32_16x16x32_bf16 v[102:105], v[170:173], v[206:209], v[102:105]
	v_mfma_f32_16x16x32_bf16 v[98:101], v[178:181], v[206:209], v[98:101]
	v_mfma_f32_16x16x32_bf16 v[86:89], v[170:173], v[214:217], v[86:89]
	v_mfma_f32_16x16x32_bf16 v[82:85], v[178:181], v[214:217], v[82:85]
	v_mfma_f32_16x16x32_bf16 v[70:73], v[170:173], v[222:225], v[70:73]
	v_mfma_f32_16x16x32_bf16 v[66:69], v[178:181], v[222:225], v[66:69]
	v_mfma_f32_16x16x32_bf16 v[120:123], v[174:177], v[202:205], v[120:123]
	v_mfma_f32_16x16x32_bf16 v[116:119], v[194:197], v[202:205], v[116:119]
	v_mfma_f32_16x16x32_bf16 v[102:105], v[174:177], v[210:213], v[102:105]
	v_mfma_f32_16x16x32_bf16 v[98:101], v[194:197], v[210:213], v[98:101]
	v_mfma_f32_16x16x32_bf16 v[86:89], v[174:177], v[218:221], v[86:89]
	v_mfma_f32_16x16x32_bf16 v[82:85], v[194:197], v[218:221], v[82:85]
	v_mfma_f32_16x16x32_bf16 v[70:73], v[174:177], v[226:229], v[70:73]
	v_mfma_f32_16x16x32_bf16 v[66:69], v[194:197], v[226:229], v[66:69]
	s_setprio 0
	s_barrier
	s_add_u32 s16, s50, 0x8000
	s_addc_u32 s17, s51, 0
	s_add_i32 s52, s65, s7
	v_lshl_add_u64 v[144:145], s[16:17], 0, v[114:115]
	s_mov_b32 m0, s52
	ds_read_b128 v[198:201], v147 offset:49152
	ds_read_b128 v[202:205], v147 offset:50176
	ds_read_b128 v[206:209], v147 offset:51200
	ds_read_b128 v[210:213], v147 offset:52224
	ds_read_b128 v[214:217], v147 offset:53248
	ds_read_b128 v[218:221], v147 offset:54272
	ds_read_b128 v[222:225], v147 offset:55296
	ds_read_b128 v[226:229], v147 offset:56320
	global_load_lds_dwordx4 v[144:145], off
	s_add_i32 m0, s52, 0x2000
	v_lshl_add_u64 v[144:145], s[16:17], 0, v[136:137]
	s_add_u32 s16, s50, 0x9000
	s_addc_u32 s17, s51, 0
	s_add_i32 s50, s66, s7
	global_load_lds_dwordx4 v[144:145], off
	v_lshl_add_u64 v[144:145], s[16:17], 0, v[114:115]
	s_mov_b32 m0, s50
	s_nop 0
	global_load_lds_dwordx4 v[144:145], off
	v_lshl_add_u64 v[144:145], s[16:17], 0, v[136:137]
	s_add_i32 m0, s50, 0x2000
	s_nop 0
	global_load_lds_dwordx4 v[144:145], off
	v_lshl_add_u64 v[144:145], s[48:49], 0, v[132:133]
	s_mov_b32 m0, s54
	s_nop 0
	global_load_lds_dwordx4 v[144:145], off
	v_lshl_add_u64 v[144:145], s[48:49], 0, v[134:135]
	s_mov_b32 m0, s55
	s_nop 0
	global_load_lds_dwordx4 v[144:145], off
	s_waitcnt vmcnt(8)
	s_waitcnt lgkmcnt(0)
	s_barrier
	s_setprio 1
	s_waitcnt lgkmcnt(0)
	v_mfma_f32_16x16x32_bf16 v[62:65], v[148:151], v[198:201], v[62:65]
	v_mfma_f32_16x16x32_bf16 v[58:61], v[158:161], v[198:201], v[58:61]
	v_mfma_f32_16x16x32_bf16 v[46:49], v[148:151], v[206:209], v[46:49]
	v_mfma_f32_16x16x32_bf16 v[42:45], v[158:161], v[206:209], v[42:45]
	v_mfma_f32_16x16x32_bf16 v[30:33], v[148:151], v[214:217], v[30:33]
	v_mfma_f32_16x16x32_bf16 v[26:29], v[158:161], v[214:217], v[26:29]
	v_mfma_f32_16x16x32_bf16 v[14:17], v[148:151], v[222:225], v[14:17]
	v_mfma_f32_16x16x32_bf16 v[10:13], v[158:161], v[222:225], v[10:13]
	v_mfma_f32_16x16x32_bf16 v[62:65], v[152:155], v[202:205], v[62:65]
	v_mfma_f32_16x16x32_bf16 v[58:61], v[166:169], v[202:205], v[58:61]
	v_mfma_f32_16x16x32_bf16 v[46:49], v[152:155], v[210:213], v[46:49]
	v_mfma_f32_16x16x32_bf16 v[42:45], v[166:169], v[210:213], v[42:45]
	v_mfma_f32_16x16x32_bf16 v[30:33], v[152:155], v[218:221], v[30:33]
	v_mfma_f32_16x16x32_bf16 v[26:29], v[166:169], v[218:221], v[26:29]
	v_mfma_f32_16x16x32_bf16 v[14:17], v[152:155], v[226:229], v[14:17]
	v_mfma_f32_16x16x32_bf16 v[10:13], v[166:169], v[226:229], v[10:13]
	s_setprio 0
	s_setprio 1
	v_mfma_f32_16x16x32_bf16 v[54:57], v[170:173], v[198:201], v[54:57]
	v_mfma_f32_16x16x32_bf16 v[50:53], v[178:181], v[198:201], v[50:53]
	v_mfma_f32_16x16x32_bf16 v[38:41], v[170:173], v[206:209], v[38:41]
	v_mfma_f32_16x16x32_bf16 v[34:37], v[178:181], v[206:209], v[34:37]
	v_mfma_f32_16x16x32_bf16 v[22:25], v[170:173], v[214:217], v[22:25]
	v_mfma_f32_16x16x32_bf16 v[18:21], v[178:181], v[214:217], v[18:21]
	v_mfma_f32_16x16x32_bf16 v[6:9], v[170:173], v[222:225], v[6:9]
	v_mfma_f32_16x16x32_bf16 v[2:5], v[178:181], v[222:225], v[2:5]
	v_mfma_f32_16x16x32_bf16 v[54:57], v[174:177], v[202:205], v[54:57]
	v_mfma_f32_16x16x32_bf16 v[50:53], v[194:197], v[202:205], v[50:53]
	v_mfma_f32_16x16x32_bf16 v[38:41], v[174:177], v[210:213], v[38:41]
	v_mfma_f32_16x16x32_bf16 v[34:37], v[194:197], v[210:213], v[34:37]
	v_mfma_f32_16x16x32_bf16 v[22:25], v[174:177], v[218:221], v[22:25]
	v_mfma_f32_16x16x32_bf16 v[18:21], v[194:197], v[218:221], v[18:21]
	v_mfma_f32_16x16x32_bf16 v[6:9], v[174:177], v[226:229], v[6:9]
	v_mfma_f32_16x16x32_bf16 v[2:5], v[194:197], v[226:229], v[2:5]
	s_setprio 0
	s_barrier
	s_add_i32 s64, s64, 2
	s_add_u32 s46, s46, 0x10000
	s_addc_u32 s47, s47, 0
	s_add_u32 s62, s62, 0x10000
	s_addc_u32 s63, s63, 0
	s_cmp_gt_u32 s64, 29
	s_cbranch_scc0 .LBB0_1230
	s_add_u32 s100, s60, 0xc000
	s_addc_u32 s101, s29, 0
	v_lshl_add_u64 v[144:145], s[100:101], 0, v[140:141]
	s_add_i32 m0, s20, 0xc000
	s_nop 0
	global_load_lds_dwordx4 v[144:145], off
	v_lshl_add_u64 v[144:145], s[100:101], 0, v[142:143]
	s_add_i32 m0, s20, 0xe000
	s_nop 0
	global_load_lds_dwordx4 v[144:145], off
	s_and_b64 vcc, exec, s[10:11]
	s_cbranch_vccz .LBB0_1233
	s_barrier

	.amdhsa_kernel _Z3fwd4Args
		.amdhsa_group_segment_fixed_size 0
		.amdhsa_private_segment_fixed_size 0
		.amdhsa_kernarg_size 416
		.amdhsa_user_sgpr_count 2
		.amdhsa_user_sgpr_dispatch_ptr 0
		.amdhsa_user_sgpr_queue_ptr 0
		.amdhsa_user_sgpr_kernarg_segment_ptr 1
		.amdhsa_user_sgpr_dispatch_id 0
		.amdhsa_user_sgpr_kernarg_preload_length 0
		.amdhsa_user_sgpr_kernarg_preload_offset 0
		.amdhsa_user_sgpr_private_segment_size 0
		.amdhsa_uses_dynamic_stack 0
		.amdhsa_enable_private_segment 0
		.amdhsa_system_sgpr_workgroup_id_x 1
		.amdhsa_system_sgpr_workgroup_id_y 0
		.amdhsa_system_sgpr_workgroup_id_z 0
		.amdhsa_system_sgpr_workgroup_info 0
		.amdhsa_system_vgpr_workitem_id 0
		.amdhsa_next_free_vgpr 256
		.amdhsa_next_free_sgpr 102
		.amdhsa_accum_offset 256
		.amdhsa_reserve_vcc 1
		.amdhsa_float_round_mode_32 0
		.amdhsa_float_round_mode_16_64 0
		.amdhsa_float_denorm_mode_32 3
		.amdhsa_float_denorm_mode_16_64 3
		.amdhsa_dx10_clamp 1
		.amdhsa_ieee_mode 1
		.amdhsa_fp16_overflow 0
		.amdhsa_tg_split 0
		.amdhsa_exception_fp_ieee_invalid_op 0
		.amdhsa_exception_fp_denorm_src 0
		.amdhsa_exception_fp_ieee_div_zero 0
		.amdhsa_exception_fp_ieee_overflow 0
		.amdhsa_exception_fp_ieee_underflow 0
		.amdhsa_exception_fp_ieee_inexact 0
		.amdhsa_exception_int_div_zero 0
	.end_amdhsa_kernel

amdhsa.kernels:
  - .agpr_count:     0
    .args:
      - .offset:         0
        .size:           160
        .value_kind:     by_value
      - .offset:         160
        .size:           4
        .value_kind:     hidden_block_count_x
      - .offset:         164
        .size:           4
        .value_kind:     hidden_block_count_y
      - .offset:         168
        .size:           4
        .value_kind:     hidden_block_count_z
      - .offset:         172
        .size:           2
        .value_kind:     hidden_group_size_x
      - .offset:         174
        .size:           2
        .value_kind:     hidden_group_size_y
      - .offset:         176
        .size:           2
        .value_kind:     hidden_group_size_z
      - .offset:         178
        .size:           2
        .value_kind:     hidden_remainder_x
      - .offset:         180
        .size:           2
        .value_kind:     hidden_remainder_y
      - .offset:         182
        .size:           2
        .value_kind:     hidden_remainder_z
      - .offset:         200
        .size:           8
        .value_kind:     hidden_global_offset_x
      - .offset:         208
        .size:           8
        .value_kind:     hidden_global_offset_y
      - .offset:         216
        .size:           8
        .value_kind:     hidden_global_offset_z
      - .offset:         224
        .size:           2
        .value_kind:     hidden_grid_dims
      - .offset:         280
        .size:           4
        .value_kind:     hidden_dynamic_lds_size
    .group_segment_fixed_size: 0
    .kernarg_segment_align: 8
    .kernarg_segment_size: 416
    .language:       OpenCL C
    .language_version:
      - 2
      - 0
    .max_flat_workgroup_size: 512
    .name:           _Z3fwd4Args
    .private_segment_fixed_size: 0
    .sgpr_count:     108
    .sgpr_spill_count: 100
    .symbol:         _Z3fwd4Args.kd
    .uniform_work_group_size: 1
    .uses_dynamic_stack: false
    .vgpr_count:     256
    .vgpr_spill_count: 0
    .wavefront_size: 64
